# v54 + P2a expert ranking: the wave's 32 cnt[e] values loaded once and broadcast by v_readlane instead of 32 dependent global loads per layer
# speedup vs baseline: 1.0128x; 1.0068x over previous
.LBB0_251:
	s_andn2_b64 vcc, exec, s[4:5]
	v_and_b32_e32 v213, 63, v0
	v_lshrrev_b32_e32 v222, 1, v0
	s_cbranch_vccnz .LBB0_293
	v_lshlrev_b32_e32 v2, 2, v213
	global_load_dword v9, v2, s[2:3]
	global_load_dword v10, v2, s[2:3] offset:256
	global_load_dword v11, v2, s[2:3] offset:512
	global_load_dword v12, v2, s[2:3] offset:768
	s_movk_i32 s22, 0x200
	v_mov_b32_e32 v4, 0xe0
	v_lshlrev_b32_e32 v2, 1, v0
	v_and_b32_e32 v2, 0x380, v2
	v_mov_b32_e32 v3, 0
	v_lshl_add_u64 v[2:3], s[2:3], 0, v[2:3]
	s_mov_b32 s23, 0
	v_or_b32_e32 v5, 64, v213
	v_or_b32_e32 v6, 0x80, v213
	v_or_b32_e32 v7, 0xc0, v213
	v_and_b32_e32 v8, 0xe0, v222
	v_cmp_eq_u32_e32 vcc, 0, v213
	v_lshl_add_u64 v[2:3], v[2:3], 0, 4
	v_and_b32_e32 v250, 31, v0
	v_lshlrev_b32_e32 v250, 2, v250
	v_lshlrev_b32_e32 v251, 1, v0
	v_and_b32_e32 v251, 0x380, v251
	v_add_u32_e32 v250, v250, v251
	global_load_dword v250, v250, s[2:3]
	s_waitcnt vmcnt(4)
	v_cmp_lt_i32_e64 s[6:7], s22, v9
	s_nop 1
	v_cndmask_b32_e64 v13, 0, v4, s[6:7]
	s_waitcnt vmcnt(3)
	v_cmp_lt_i32_e64 s[6:7], s22, v10
	v_add_u32_e32 v9, v13, v9
	s_nop 0
	v_cndmask_b32_e64 v14, 0, v4, s[6:7]
	s_waitcnt vmcnt(2)
	v_cmp_lt_i32_e64 s[6:7], s22, v11
	v_add_u32_e32 v10, v14, v10
	s_nop 0
	v_cndmask_b32_e64 v15, 0, v4, s[6:7]
	s_waitcnt vmcnt(1)
	v_cmp_lt_i32_e64 s[6:7], s22, v12
	v_add_u32_e32 v11, v15, v11
	s_nop 0
	v_cndmask_b32_e64 v16, 0, v4, s[6:7]
	v_add_u32_e32 v12, v16, v12
	s_waitcnt vmcnt(0)
	s_branch .LBB0_254

.LBB0_254:
	s_nop 3
	v_readlane_b32 s98, v250, s23
	v_add_u32_e32 v13, s23, v8
	v_cmp_lt_u32_e64 s[6:7], v213, v13
	v_cmp_lt_u32_e64 s[8:9], v5, v13
	v_cmp_lt_u32_e64 s[10:11], v6, v13
	v_cmp_lt_u32_e64 s[12:13], v7, v13
	v_mov_b32_e32 v14, s98
	v_cmp_lt_i32_e64 s[14:15], s22, v14
	s_nop 1
	v_cndmask_b32_e64 v15, 0, v4, s[14:15]
	v_add_u32_e32 v14, v15, v14
	v_cmp_eq_u32_e64 s[16:17], v9, v14
	v_cmp_gt_i32_e64 s[14:15], v9, v14
	v_cmp_eq_u32_e64 s[20:21], v10, v14
	s_and_b64 s[4:5], s[16:17], s[6:7]
	v_cmp_gt_i32_e64 s[18:19], v10, v14
	v_cmp_eq_u32_e64 s[26:27], v11, v14
	s_and_b64 s[6:7], s[20:21], s[8:9]
	s_or_b64 s[4:5], s[14:15], s[4:5]
	v_cmp_gt_i32_e64 s[24:25], v11, v14
	v_cmp_gt_i32_e64 s[28:29], v12, v14
	v_cmp_eq_u32_e64 s[30:31], v12, v14
	s_and_b64 s[8:9], s[26:27], s[10:11]
	v_cndmask_b32_e64 v14, 0, 1, s[4:5]
	s_or_b64 s[4:5], s[18:19], s[6:7]
	s_and_b64 s[10:11], s[30:31], s[12:13]
	v_cndmask_b32_e64 v15, 0, 1, s[4:5]
	s_or_b64 s[4:5], s[24:25], s[8:9]
	v_cndmask_b32_e64 v16, 0, 1, s[4:5]
	s_or_b64 s[4:5], s[28:29], s[10:11]
	v_cndmask_b32_e64 v17, 0, 1, s[4:5]
	v_cmp_ne_u32_e64 s[6:7], 0, v14
	v_cmp_ne_u32_e64 s[8:9], 0, v15
	v_cmp_ne_u32_e64 s[10:11], 0, v16
	v_cmp_ne_u32_e64 s[12:13], 0, v17
	s_and_saveexec_b64 s[4:5], vcc
	s_cbranch_execz .LBB0_256
	s_bcnt1_i32_b64 s6, s[6:7]
	s_bcnt1_i32_b64 s7, s[8:9]
	s_lshl_b32 s6, s6, 2
	s_bcnt1_i32_b64 s8, s[10:11]
	s_add_i32 s6, s6, 0
	s_lshl_b32 s7, s7, 2
	s_bcnt1_i32_b64 s9, s[12:13]
	s_add_i32 s6, s6, s7
	s_lshl_b32 s7, s8, 2
	s_add_i32 s6, s6, s7
	s_lshl_b32 s7, s9, 2
	s_add_i32 s6, s6, s7
	s_add_i32 s6, s6, 0x21400
	v_mov_b32_e32 v14, s6
	ds_write_b32 v14, v13
.LBB0_256:
	s_or_b64 exec, exec, s[4:5]
	s_add_i32 s99, s23, 1
	s_nop 3
	v_readlane_b32 s98, v250, s99
	v_cmp_le_u32_e64 s[6:7], v213, v13
	v_cmp_le_u32_e64 s[8:9], v5, v13
	v_cmp_le_u32_e64 s[10:11], v6, v13
	v_cmp_le_u32_e64 s[12:13], v7, v13
	v_mov_b32_e32 v14, s98
	v_cmp_lt_i32_e64 s[14:15], s22, v14
	s_nop 1
	v_cndmask_b32_e64 v15, 0, v4, s[14:15]
	v_add_u32_e32 v14, v15, v14
	v_cmp_eq_u32_e64 s[16:17], v9, v14
	v_cmp_gt_i32_e64 s[14:15], v9, v14
	v_cmp_eq_u32_e64 s[20:21], v10, v14
	s_and_b64 s[4:5], s[16:17], s[6:7]
	v_cmp_gt_i32_e64 s[18:19], v10, v14
	v_cmp_eq_u32_e64 s[26:27], v11, v14
	s_and_b64 s[6:7], s[20:21], s[8:9]
	s_or_b64 s[4:5], s[14:15], s[4:5]
	v_cmp_gt_i32_e64 s[24:25], v11, v14
	v_cmp_gt_i32_e64 s[28:29], v12, v14
	v_cmp_eq_u32_e64 s[30:31], v12, v14
	s_and_b64 s[8:9], s[26:27], s[10:11]
	v_cndmask_b32_e64 v14, 0, 1, s[4:5]
	s_or_b64 s[4:5], s[18:19], s[6:7]
	s_and_b64 s[10:11], s[30:31], s[12:13]
	v_cndmask_b32_e64 v15, 0, 1, s[4:5]
	s_or_b64 s[4:5], s[24:25], s[8:9]
	v_cndmask_b32_e64 v16, 0, 1, s[4:5]
	s_or_b64 s[4:5], s[28:29], s[10:11]
	v_cndmask_b32_e64 v17, 0, 1, s[4:5]
	v_cmp_ne_u32_e64 s[6:7], 0, v14
	v_cmp_ne_u32_e64 s[8:9], 0, v15
	v_cmp_ne_u32_e64 s[10:11], 0, v16
	v_cmp_ne_u32_e64 s[12:13], 0, v17
	s_and_saveexec_b64 s[4:5], vcc
	s_cbranch_execz .LBB0_253
	s_bcnt1_i32_b64 s6, s[6:7]
	s_bcnt1_i32_b64 s7, s[8:9]
	s_lshl_b32 s6, s6, 2
	s_bcnt1_i32_b64 s8, s[10:11]
	s_add_i32 s6, s6, 0
	s_lshl_b32 s7, s7, 2
	s_bcnt1_i32_b64 s9, s[12:13]
	s_add_i32 s6, s6, s7
	s_lshl_b32 s7, s8, 2
	s_add_i32 s6, s6, s7
	s_lshl_b32 s7, s9, 2
	s_add_i32 s6, s6, s7
	s_add_i32 s6, s6, 0x21400
	v_add_u32_e32 v13, 1, v13
	v_mov_b32_e32 v14, s6
	ds_write_b32 v14, v13
	s_branch .LBB0_253

.LBB0_857:
	s_andn2_b64 vcc, exec, s[4:5]
	s_cbranch_vccnz .LBB0_899
	v_lshlrev_b32_e32 v2, 2, v213
	global_load_dword v9, v2, s[2:3] offset:1024
	global_load_dword v10, v2, s[2:3] offset:1280
	global_load_dword v11, v2, s[2:3] offset:1536
	global_load_dword v12, v2, s[2:3] offset:1792
	s_movk_i32 s6, 0x200
	v_mov_b32_e32 v4, 0xe0
	v_lshlrev_b32_e32 v2, 1, v0
	v_and_b32_e32 v2, 0x380, v2
	v_mov_b32_e32 v3, 0
	s_mov_b64 s[4:5], 0x400
	v_lshl_add_u64 v[2:3], s[2:3], 0, v[2:3]
	s_mov_b32 s7, 0
	v_or_b32_e32 v5, 64, v213
	v_or_b32_e32 v6, 0x80, v213
	v_or_b32_e32 v7, 0xc0, v213
	v_and_b32_e32 v8, 0xe0, v222
	v_cmp_eq_u32_e32 vcc, 0, v213
	v_lshl_add_u64 v[2:3], v[2:3], 0, s[4:5]
	v_and_b32_e32 v250, 31, v0
	v_lshlrev_b32_e32 v250, 2, v250
	v_lshlrev_b32_e32 v251, 1, v0
	v_and_b32_e32 v251, 0x380, v251
	v_add_u32_e32 v250, v250, v251
	global_load_dword v250, v250, s[2:3] offset:1024
	s_waitcnt vmcnt(4)
	v_cmp_lt_i32_e64 s[10:11], s6, v9
	s_nop 1
	v_cndmask_b32_e64 v13, 0, v4, s[10:11]
	s_waitcnt vmcnt(3)
	v_cmp_lt_i32_e64 s[10:11], s6, v10
	v_add_u32_e32 v9, v13, v9
	s_nop 0
	v_cndmask_b32_e64 v14, 0, v4, s[10:11]
	s_waitcnt vmcnt(2)
	v_cmp_lt_i32_e64 s[10:11], s6, v11
	v_add_u32_e32 v10, v14, v10
	s_nop 0
	v_cndmask_b32_e64 v15, 0, v4, s[10:11]
	s_waitcnt vmcnt(1)
	v_cmp_lt_i32_e64 s[10:11], s6, v12
	v_add_u32_e32 v11, v15, v11
	s_nop 0
	v_cndmask_b32_e64 v16, 0, v4, s[10:11]
	v_add_u32_e32 v12, v16, v12
	s_waitcnt vmcnt(0)
	s_branch .LBB0_860

.LBB0_860:
	s_nop 3
	v_readlane_b32 s98, v250, s7
	v_add_u32_e32 v13, s7, v8
	v_cmp_lt_u32_e64 s[10:11], v213, v13
	v_cmp_lt_u32_e64 s[12:13], v5, v13
	v_cmp_lt_u32_e64 s[14:15], v6, v13
	v_cmp_lt_u32_e64 s[16:17], v7, v13
	v_mov_b32_e32 v14, s98
	v_cmp_lt_i32_e64 s[18:19], s6, v14
	s_nop 1
	v_cndmask_b32_e64 v15, 0, v4, s[18:19]
	v_add_u32_e32 v14, v15, v14
	v_cmp_eq_u32_e64 s[20:21], v9, v14
	v_cmp_gt_i32_e64 s[18:19], v9, v14
	v_cmp_eq_u32_e64 s[26:27], v10, v14
	s_and_b64 s[4:5], s[20:21], s[10:11]
	v_cmp_gt_i32_e64 s[24:25], v10, v14
	v_cmp_eq_u32_e64 s[30:31], v11, v14
	s_and_b64 s[8:9], s[26:27], s[12:13]
	s_or_b64 s[4:5], s[18:19], s[4:5]
	v_cmp_gt_i32_e64 s[28:29], v11, v14
	v_cmp_gt_i32_e64 s[34:35], v12, v14
	v_cmp_eq_u32_e64 s[36:37], v12, v14
	s_and_b64 s[10:11], s[30:31], s[14:15]
	v_cndmask_b32_e64 v14, 0, 1, s[4:5]
	s_or_b64 s[4:5], s[24:25], s[8:9]
	s_and_b64 s[12:13], s[36:37], s[16:17]
	v_cndmask_b32_e64 v15, 0, 1, s[4:5]
	s_or_b64 s[4:5], s[28:29], s[10:11]
	v_cndmask_b32_e64 v16, 0, 1, s[4:5]
	s_or_b64 s[4:5], s[34:35], s[12:13]
	v_cndmask_b32_e64 v17, 0, 1, s[4:5]
	v_cmp_ne_u32_e64 s[10:11], 0, v14
	v_cmp_ne_u32_e64 s[12:13], 0, v15
	v_cmp_ne_u32_e64 s[14:15], 0, v16
	v_cmp_ne_u32_e64 s[16:17], 0, v17
	s_and_saveexec_b64 s[4:5], vcc
	s_cbranch_execz .LBB0_862
	s_bcnt1_i32_b64 s8, s[10:11]
	s_bcnt1_i32_b64 s9, s[12:13]
	s_lshl_b32 s8, s8, 2
	s_bcnt1_i32_b64 s10, s[14:15]
	s_add_i32 s8, s8, 0
	s_lshl_b32 s9, s9, 2
	s_bcnt1_i32_b64 s11, s[16:17]
	s_add_i32 s8, s8, s9
	s_lshl_b32 s9, s10, 2
	s_add_i32 s8, s8, s9
	s_lshl_b32 s9, s11, 2
	s_add_i32 s8, s8, s9
	s_add_i32 s8, s8, 0x21400
	v_mov_b32_e32 v14, s8
	ds_write_b32 v14, v13
.LBB0_862:
	s_or_b64 exec, exec, s[4:5]
	s_add_i32 s99, s7, 1
	s_nop 3
	v_readlane_b32 s98, v250, s99
	v_cmp_le_u32_e64 s[10:11], v213, v13
	v_cmp_le_u32_e64 s[12:13], v5, v13
	v_cmp_le_u32_e64 s[14:15], v6, v13
	v_cmp_le_u32_e64 s[16:17], v7, v13
	v_mov_b32_e32 v14, s98
	v_cmp_lt_i32_e64 s[18:19], s6, v14
	s_nop 1
	v_cndmask_b32_e64 v15, 0, v4, s[18:19]
	v_add_u32_e32 v14, v15, v14
	v_cmp_eq_u32_e64 s[20:21], v9, v14
	v_cmp_gt_i32_e64 s[18:19], v9, v14
	v_cmp_eq_u32_e64 s[26:27], v10, v14
	s_and_b64 s[4:5], s[20:21], s[10:11]
	v_cmp_gt_i32_e64 s[24:25], v10, v14
	v_cmp_eq_u32_e64 s[30:31], v11, v14
	s_and_b64 s[8:9], s[26:27], s[12:13]
	s_or_b64 s[4:5], s[18:19], s[4:5]
	v_cmp_gt_i32_e64 s[28:29], v11, v14
	v_cmp_gt_i32_e64 s[34:35], v12, v14
	v_cmp_eq_u32_e64 s[36:37], v12, v14
	s_and_b64 s[10:11], s[30:31], s[14:15]
	v_cndmask_b32_e64 v14, 0, 1, s[4:5]
	s_or_b64 s[4:5], s[24:25], s[8:9]
	s_and_b64 s[12:13], s[36:37], s[16:17]
	v_cndmask_b32_e64 v15, 0, 1, s[4:5]
	s_or_b64 s[4:5], s[28:29], s[10:11]
	v_cndmask_b32_e64 v16, 0, 1, s[4:5]
	s_or_b64 s[4:5], s[34:35], s[12:13]
	v_cndmask_b32_e64 v17, 0, 1, s[4:5]
	v_cmp_ne_u32_e64 s[10:11], 0, v14
	v_cmp_ne_u32_e64 s[12:13], 0, v15
	v_cmp_ne_u32_e64 s[14:15], 0, v16
	v_cmp_ne_u32_e64 s[16:17], 0, v17
	s_and_saveexec_b64 s[4:5], vcc
	s_cbranch_execz .LBB0_859
	s_bcnt1_i32_b64 s8, s[10:11]
	s_bcnt1_i32_b64 s9, s[12:13]
	s_lshl_b32 s8, s8, 2
	s_bcnt1_i32_b64 s10, s[14:15]
	s_add_i32 s8, s8, 0
	s_lshl_b32 s9, s9, 2
	s_bcnt1_i32_b64 s11, s[16:17]
	s_add_i32 s8, s8, s9
	s_lshl_b32 s9, s10, 2
	s_add_i32 s8, s8, s9
	s_lshl_b32 s9, s11, 2
	s_add_i32 s8, s8, s9
	s_add_i32 s8, s8, 0x21400
	v_add_u32_e32 v13, 1, v13
	v_mov_b32_e32 v14, s8
	ds_write_b32 v14, v13
	s_branch .LBB0_859
